# v18 + down-phase unit permutation with XCD-local gate|up->down barrier; arrival atomic issued before the L1 invalidate (wait only for the atomic); local release without waiting for own invalidate
# speedup vs baseline: 1.0567x; 1.0033x over previous
.LBB0_781:
	v_readlane_b32 s6, v254, 17
	v_readlane_b32 s7, v254, 18
	v_cvt_f32_u32_e32 v1, v2
	v_sub_u32_e32 v4, 0, v2
	v_rcp_iflag_f32_e32 v1, v1
	s_nop 1
	global_atomic_add v3, v65, v167, s[6:7] sc0
	buffer_inv sc1
	v_mul_f32_e32 v1, 0x4f7ffffe, v1
	v_cvt_u32_f32_e32 v1, v1
	v_mul_lo_u32 v4, v4, v1
	v_mul_hi_u32 v4, v1, v4
	v_add_u32_e32 v1, v1, v4
	s_waitcnt vmcnt(1)
	v_mul_hi_u32 v1, v3, v1
	v_mul_lo_u32 v4, v1, v2
	v_sub_u32_e32 v4, v3, v4
	v_add_u32_e32 v5, 1, v1
	v_cmp_ge_u32_e32 vcc, v4, v2
	v_add_u32_e32 v3, 1, v3
	s_nop 0
	v_cndmask_b32_e32 v1, v1, v5, vcc
	v_sub_u32_e32 v5, v4, v2
	v_cndmask_b32_e32 v4, v4, v5, vcc
	v_add_u32_e32 v5, 1, v1
	v_cmp_ge_u32_e32 vcc, v4, v2
	s_nop 1
	v_cndmask_b32_e32 v1, v1, v5, vcc
	v_mul_lo_u32 v4, v2, v1
	v_add_u32_e32 v2, v4, v2
	v_cmp_ne_u32_e32 vcc, v3, v2
	s_and_saveexec_b64 s[6:7], vcc
	s_xor_b64 s[6:7], exec, s[6:7]
	s_cbranch_execz .LBB0_795
	v_readlane_b32 s8, v254, 19
	v_readlane_b32 s9, v254, 20
	s_waitcnt lgkmcnt(0)
	s_nop 3
	global_load_dword v0, v65, s[8:9] sc1
	s_waitcnt vmcnt(0)
	v_cmp_eq_u32_e32 vcc, v0, v1
	s_and_saveexec_b64 s[8:9], vcc
	s_cbranch_execz .LBB0_794
	s_mov_b32 s21, 1
	s_mov_b64 s[10:11], 0
	s_branch .LBB0_785

.LBB0_795:
	s_andn2_saveexec_b64 s[6:7], s[6:7]
	s_cbranch_execz .LBB0_813
	s_mov_b64 s[6:7], exec
	v_readlane_b32 s8, v255, 50
	s_nop 3
	s_cmp_eq_u32 s8, 1
	s_cbranch_scc0 .Lxg_814
	s_waitcnt lgkmcnt(0)
	v_readlane_b32 s6, v254, 19
	v_readlane_b32 s7, v254, 20
	s_nop 5
	global_atomic_add v65, v167, s[6:7]
	s_branch .Lxa_814

.LBB0_812:
	s_or_b64 exec, exec, s[6:7]
	v_readlane_b32 s6, v254, 19
	v_readlane_b32 s7, v254, 20
	s_waitcnt vmcnt(0)
	s_nop 3
	global_atomic_add v65, v167, s[6:7]
.Lxa_814:
	s_waitcnt vmcnt(0)
.LBB0_813:
	s_or_b64 exec, exec, s[4:5]
	s_waitcnt lgkmcnt(0)
	s_barrier

.LBB0_947:
	s_or_b64 exec, exec, s[6:7]
	v_readlane_b32 s6, v254, 19
	v_readlane_b32 s7, v254, 20
	s_waitcnt vmcnt(0)
	s_nop 3
	global_atomic_add v65, v167, s[6:7]
.Lxa_949:
	s_waitcnt vmcnt(0)
.LBB0_948:
	s_or_b64 exec, exec, s[4:5]
	s_waitcnt lgkmcnt(0)
	s_barrier

.LBB0_1355:
	s_or_b64 exec, exec, s[6:7]
	v_readlane_b32 s6, v254, 19
	v_readlane_b32 s7, v254, 20
	s_waitcnt vmcnt(0)
	s_nop 3
	global_atomic_add v65, v167, s[6:7]
.Lxa_1357:
	s_waitcnt vmcnt(0)
.LBB0_1356:
	s_or_b64 exec, exec, s[4:5]
	s_waitcnt lgkmcnt(0)
	s_barrier

.LBB0_1639:
	s_or_b64 exec, exec, s[6:7]
	v_readlane_b32 s6, v254, 19
	v_readlane_b32 s7, v254, 20
	s_waitcnt vmcnt(0)
	s_nop 3
	global_atomic_add v65, v167, s[6:7]
.Lxa_1641:
	s_waitcnt vmcnt(0)
.LBB0_1640:
	s_or_b64 exec, exec, s[4:5]
	s_waitcnt lgkmcnt(0)
	s_barrier

.LBB0_1700:
	s_or_b64 exec, exec, s[6:7]
	v_readlane_b32 s6, v254, 19
	v_readlane_b32 s7, v254, 20
	s_waitcnt vmcnt(0)
	s_nop 3
	global_atomic_add v65, v167, s[6:7]
.Lxa_1702:
	s_waitcnt vmcnt(0)
.LBB0_1701:
	s_or_b64 exec, exec, s[4:5]
	s_waitcnt lgkmcnt(0)
	s_barrier

.LBB0_1837:
	s_or_b64 exec, exec, s[6:7]
	v_readlane_b32 s6, v254, 19
	v_readlane_b32 s7, v254, 20
	s_waitcnt vmcnt(0)
	s_nop 3
	global_atomic_add v65, v167, s[6:7]
.Lxa_1839:
	s_waitcnt vmcnt(0)
.LBB0_1838:
	s_or_b64 exec, exec, s[4:5]
	s_waitcnt lgkmcnt(0)
	s_barrier

.LBB0_1910:
	s_or_b64 exec, exec, s[6:7]
	v_readlane_b32 s6, v254, 19
	v_readlane_b32 s7, v254, 20
	s_waitcnt vmcnt(0)
	s_nop 3
	global_atomic_add v65, v167, s[6:7]
.Lxa_1912:
	s_waitcnt vmcnt(0)
.LBB0_1911:
	s_or_b64 exec, exec, s[4:5]
	s_waitcnt lgkmcnt(0)
	s_barrier

.LBB0_2402:
	s_or_b64 exec, exec, s[6:7]
	v_readlane_b32 s6, v254, 19
	v_readlane_b32 s7, v254, 20
	s_waitcnt vmcnt(0)
	s_nop 3
	global_atomic_add v65, v167, s[6:7]
.Lxa_2404:
	s_waitcnt vmcnt(0)
.LBB0_2403:
	s_or_b64 exec, exec, s[4:5]
	s_waitcnt lgkmcnt(0)
	s_barrier

.LBB0_2416:
	v_readlane_b32 s4, v255, 0
	s_mov_b32 s5, 0x3fffe0
	v_mov_b32_e32 v186, 0x7d
	v_mov_b32_e32 v0, s4
	ds_read_b32 v0, v0
	v_mov_b32_e32 v187, 0x79
	v_bfe_i32 v2, v8, 27, 1
	v_lshrrev_b32_e32 v2, 22, v2
	s_waitcnt lgkmcnt(0)
	v_readfirstlane_b32 s4, v0
	v_lshlrev_b32_e32 v0, 4, v8
	v_add_u32_e32 v2, v0, v2
	v_and_b32_e32 v2, 0xfffffc00, v2
	v_sub_u32_e32 v2, v0, v2
	v_ashrrev_i32_e32 v1, 31, v8
	v_lshrrev_b32_e32 v3, 4, v2
	v_lshrrev_b32_e32 v1, 26, v1
	v_bitop3_b32 v2, v3, v2, 32 bitop3:0x6c
	v_add_u32_e32 v1, v8, v1
	v_ashrrev_i32_e32 v4, 31, v2
	v_ashrrev_i32_e32 v1, 6, v1
	v_lshrrev_b32_e32 v4, 26, v4
	v_lshlrev_b32_e32 v3, 3, v1
	v_add_u32_e32 v4, v2, v4
	v_and_b32_e32 v3, -16, v3
	v_ashrrev_i32_e32 v5, 6, v4
	v_and_b32_e32 v4, 0xc0, v4
	v_add_u32_e32 v3, v5, v3
	v_sub_u32_e32 v2, v2, v4
	v_lshlrev_b32_e32 v1, 5, v1
	v_ashrrev_i16_sdwa v2, v167, sext(v2) dst_sel:DWORD dst_unused:UNUSED_PAD src0_sel:DWORD src1_sel:BYTE_0
	v_lshlrev_b32_e32 v4, 1, v3
	v_lshrrev_b32_e32 v6, 2, v3
	v_and_b32_e32 v5, 3, v5
	v_and_b32_e32 v1, 32, v1
	v_bfe_i32 v2, v2, 0, 16
	v_and_b32_e32 v4, 24, v4
	v_and_b32_e32 v6, 4, v6
	v_and_or_b32 v5, v3, s5, v5
	v_or3_b32 v4, v5, v6, v4
	v_add_lshl_u32 v1, v1, v2, 1
	v_add_u32_e32 v0, 0x2000, v0
	v_lshl_add_u32 v172, v3, 10, v1
	v_lshl_add_u32 v64, v4, 10, v1
	v_ashrrev_i32_e32 v1, 31, v0
	v_lshrrev_b32_e32 v1, 22, v1
	v_add_u32_e32 v1, v0, v1
	v_ashrrev_i32_e32 v1, 10, v1
	v_mul_i32_i24_e32 v2, 0x400, v1
	v_sub_u32_e32 v0, v0, v2
	v_lshrrev_b32_e32 v2, 4, v0
	v_bitop3_b32 v0, v2, v0, 32 bitop3:0x6c
	v_ashrrev_i32_e32 v3, 31, v0
	v_lshrrev_b32_e32 v3, 26, v3
	v_lshlrev_b32_e32 v2, 3, v1
	v_add_u32_e32 v3, v0, v3
	v_and_b32_e32 v2, -16, v2
	v_ashrrev_i32_e32 v4, 6, v3
	v_and_b32_e32 v3, 0xc0, v3
	v_add_u32_e32 v2, v4, v2
	v_sub_u32_e32 v0, v0, v3
	v_lshlrev_b32_e32 v1, 5, v1
	v_ashrrev_i16_sdwa v0, v167, sext(v0) dst_sel:DWORD dst_unused:UNUSED_PAD src0_sel:DWORD src1_sel:BYTE_0
	v_lshlrev_b32_e32 v3, 1, v2
	v_lshrrev_b32_e32 v5, 2, v2
	v_and_b32_e32 v4, 3, v4
	v_and_b32_e32 v1, 32, v1
	v_bfe_i32 v0, v0, 0, 16
	v_and_b32_e32 v3, 24, v3
	v_and_b32_e32 v5, 4, v5
	v_and_or_b32 v4, v2, s5, v4
	v_or3_b32 v3, v4, v5, v3
	v_add_lshl_u32 v0, v1, v0, 1
	s_lshl_b32 s26, s4, 2
	v_readfirstlane_b32 s10, v8
	v_lshl_add_u32 v174, v2, 10, v0
	v_lshl_add_u32 v176, v3, 10, v0
	s_cmpk_lg_u32 s91, 0x100
	s_cbranch_scc1 .Ldn_nomap
	s_lshr_b32 s12, s93, 5
	s_and_b32 s13, s93, 31
	s_lshl_b32 s12, s12, 4
	s_and_b32 s14, s13, 15
	s_lshr_b32 s13, s13, 4
	s_lshl_b32 s13, s13, 7
	s_add_i32 s93, s12, s13
	s_add_i32 s93, s93, s14
.Ldn_nomap:
	s_cmp_ge_i32 s93, s26
	s_cbranch_scc1 .LBB0_2432
	s_ashr_i32 s11, s10, 6
	s_ashr_i32 s12, s10, 8
	s_lshl_b32 s27, s11, 10
	s_add_u32 s33, s6, 0x95600000
	v_readlane_b32 s4, v255, 4
	s_addc_u32 s46, s7, 0
	v_readlane_b32 s5, v255, 5
	s_lshl_b32 s34, s4, 15
	s_lshl_b64 s[4:5], s[34:35], 10
	s_add_u32 s4, s6, s4
	s_addc_u32 s5, s7, s5
	s_add_u32 s47, s4, 0x28000000
	s_addc_u32 s48, s5, 0
	s_ashr_i32 s4, s93, 31
	s_lshr_b32 s4, s4, 30
	s_add_i32 s4, s93, s4
	s_ashr_i32 s22, s4, 2
	s_and_b32 s4, s4, -4
	s_sub_i32 s13, s93, s4
	s_add_i32 s4, s4, 0
	s_add_i32 s14, s4, 0x20040
	v_mov_b32_e32 v0, s14
	ds_read_b32 v0, v0
	s_ashr_i32 s23, s22, 31
	s_lshl_b64 s[4:5], s[22:23], 18
	s_add_u32 s40, s33, s4
	s_addc_u32 s41, s46, s5
	s_add_u32 s4, s40, 0x20000
	s_waitcnt lgkmcnt(0)
	v_readfirstlane_b32 s14, v0
	s_addc_u32 s5, s41, 0
	s_lshl_b32 s14, s14, 2
	s_add_i32 s24, s14, s13
	s_ashr_i32 s25, s24, 31
	s_lshl_b64 s[14:15], s[24:25], 18
	s_add_u32 s42, s47, s14
	s_addc_u32 s43, s48, s15
	s_add_i32 s25, s27, 0
	s_add_i32 m0, s25, 0x10000
	v_mov_b32_e32 v177, v65
	global_load_lds_dwordx4 v64, s[42:43]
	s_add_i32 m0, s25, 0x12000
	s_add_u32 s14, s42, 0x20000
	global_load_lds_dwordx4 v176, s[42:43]
	s_addc_u32 s15, s43, 0
	s_add_i32 m0, s25, 0x14000
	s_add_i32 s49, s25, 0x2000
	global_load_lds_dwordx4 v64, s[14:15]
	s_add_i32 m0, s25, 0x16000
	s_add_i32 s50, s25, 0x4000
	global_load_lds_dwordx4 v176, s[14:15]
	s_mov_b32 m0, s25
	s_add_i32 s51, s25, 0x6000
	global_load_lds_dwordx4 v172, s[40:41]
	s_mov_b32 m0, s49
	v_mov_b32_e32 v173, v65
	global_load_lds_dwordx4 v174, s[40:41]
	s_mov_b32 m0, s50
	v_mov_b32_e32 v175, v65
	global_load_lds_dwordx4 v172, s[4:5]
	s_mov_b32 m0, s51
	s_cmp_eq_u32 s12, 1
	global_load_lds_dwordx4 v174, s[4:5]
	v_lshl_add_u64 v[6:7], s[42:43], 0, v[64:65]
	v_lshl_add_u64 v[4:5], s[42:43], 0, v[176:177]
	v_lshl_add_u64 v[0:1], s[40:41], 0, v[172:173]
	s_cselect_b64 s[4:5], -1, 0
	s_cmp_lg_u32 s12, 1
	v_lshl_add_u64 v[2:3], s[40:41], 0, v[174:175]
	s_cbranch_scc1 .LBB0_2419
	s_barrier

.Lpb_back:
.Lpb_done:
	s_cmpk_lg_u32 s91, 0x100
	s_cbranch_scc1 .Ldn_norest
	v_readlane_b32 s4, v255, 2
	s_nop 3
	s_and_b32 s5, s4, 7
	s_lshl_b32 s5, s5, 5
	s_lshr_b32 s4, s4, 3
	s_add_i32 s93, s5, s4

.LBB0_2518:
	v_readlane_b32 s6, v254, 17
	v_readlane_b32 s7, v254, 18
	v_cvt_f32_u32_e32 v1, v2
	v_sub_u32_e32 v4, 0, v2
	v_rcp_iflag_f32_e32 v1, v1
	s_nop 1
	global_atomic_add v3, v65, v167, s[6:7] sc0
	buffer_inv sc1
	v_mul_f32_e32 v1, 0x4f7ffffe, v1
	v_cvt_u32_f32_e32 v1, v1
	v_mul_lo_u32 v4, v4, v1
	v_mul_hi_u32 v4, v1, v4
	v_add_u32_e32 v1, v1, v4
	s_waitcnt vmcnt(1)
	v_mul_hi_u32 v1, v3, v1
	v_mul_lo_u32 v4, v1, v2
	v_sub_u32_e32 v4, v3, v4
	v_add_u32_e32 v5, 1, v1
	v_cmp_ge_u32_e32 vcc, v4, v2
	v_add_u32_e32 v3, 1, v3
	s_nop 0
	v_cndmask_b32_e32 v1, v1, v5, vcc
	v_sub_u32_e32 v5, v4, v2
	v_cndmask_b32_e32 v4, v4, v5, vcc
	v_add_u32_e32 v5, 1, v1
	v_cmp_ge_u32_e32 vcc, v4, v2
	s_nop 1
	v_cndmask_b32_e32 v1, v1, v5, vcc
	v_mul_lo_u32 v4, v2, v1
	v_add_u32_e32 v2, v4, v2
	v_cmp_ne_u32_e32 vcc, v3, v2
	s_and_saveexec_b64 s[6:7], vcc
	s_xor_b64 s[6:7], exec, s[6:7]
	s_cbranch_execz .LBB0_2532
	v_readlane_b32 s8, v254, 19
	v_readlane_b32 s9, v254, 20
	s_waitcnt lgkmcnt(0)
	s_nop 3
	global_load_dword v0, v65, s[8:9] sc1
	s_waitcnt vmcnt(0)
	v_cmp_eq_u32_e32 vcc, v0, v1
	s_and_saveexec_b64 s[8:9], vcc
	s_cbranch_execz .LBB0_2531
	s_mov_b32 s20, 1
	s_mov_b64 s[10:11], 0
	s_branch .LBB0_2522

.LBB0_2532:
	s_andn2_saveexec_b64 s[6:7], s[6:7]
	s_cbranch_execnz .LBB0_2533
.Lxf_last:
	s_getpc_b64 s[98:99]

.LBB0_2533:
	s_mov_b64 s[6:7], exec
	v_readlane_b32 s8, v255, 50
	s_nop 3
	s_cmp_eq_u32 s8, 1
	s_cbranch_scc0 .Lxg_last
	s_waitcnt lgkmcnt(0)
	v_readlane_b32 s6, v254, 19
	v_readlane_b32 s7, v254, 20
	s_nop 5
	global_atomic_add v65, v167, s[6:7]
	s_waitcnt vmcnt(0)
	s_branch .Lxf_last
